# lever 4: static s_setprio 1 for the younger wave half (waves 4-7) in the two proj GEMM main K loops, per-segment priority flips deleted there
# speedup vs baseline: 1.0039x; 1.0039x over previous
.LBB0_270:
	ds_read_b128 v[0:3], v153
	ds_read_b128 v[4:7], v153 offset:1024
	ds_read_b128 v[8:11], v153 offset:2048
	ds_read_b128 v[12:15], v153 offset:3072
	ds_read_b128 v[16:19], v154
	ds_read_b128 v[20:23], v154 offset:1024
	ds_read_b128 v[24:27], v154 offset:2048
	ds_read_b128 v[28:31], v154 offset:3072
	s_add_u32 s34, s28, 0x40080
	s_addc_u32 s35, s29, 0
	s_add_i32 s19, s43, 0xc000
	v_lshl_add_u64 v[64:65], s[34:35], 0, v[134:135]
	s_mov_b32 m0, s19
	s_add_i32 s21, s43, 0xe000
	ds_read_b128 v[32:35], v155
	ds_read_b128 v[36:39], v155 offset:1024
	ds_read_b128 v[40:43], v155 offset:2048
	ds_read_b128 v[44:47], v155 offset:3072
	ds_read_b128 v[48:51], v155 offset:4096
	ds_read_b128 v[52:55], v155 offset:5120
	ds_read_b128 v[56:59], v155 offset:6144
	ds_read_b128 v[60:63], v155 offset:7168
	global_load_lds_dwordx4 v[64:65], off
	v_lshl_add_u64 v[64:65], s[34:35], 0, v[130:131]
	s_mov_b32 m0, s21
	s_nop 0
	global_load_lds_dwordx4 v[64:65], off
	s_waitcnt vmcnt(24)
	s_waitcnt lgkmcnt(0)
	s_barrier
	s_setprio 1
	s_waitcnt lgkmcnt(0)
	v_mfma_f32_16x16x32_bf16 v[84:87], v[8:11], v[48:51], 0
	v_mfma_f32_16x16x32_bf16 v[88:91], v[12:15], v[52:55], v[84:87]
	v_mfma_f32_16x16x32_bf16 v[84:87], v[0:3], v[56:59], 0
	v_mfma_f32_16x16x32_bf16 v[64:67], v[0:3], v[32:35], 0
	v_mfma_f32_16x16x32_bf16 v[68:71], v[8:11], v[32:35], 0
	v_mfma_f32_16x16x32_bf16 v[72:75], v[0:3], v[40:43], 0
	v_mfma_f32_16x16x32_bf16 v[76:79], v[8:11], v[40:43], 0
	v_mfma_f32_16x16x32_bf16 v[80:83], v[0:3], v[48:51], 0
	v_mfma_f32_16x16x32_bf16 v[92:95], v[4:7], v[60:63], v[84:87]
	v_mfma_f32_16x16x32_bf16 v[84:87], v[8:11], v[56:59], 0
	v_mfma_f32_16x16x32_bf16 v[64:67], v[4:7], v[36:39], v[64:67]
	v_mfma_f32_16x16x32_bf16 v[68:71], v[12:15], v[36:39], v[68:71]
	v_mfma_f32_16x16x32_bf16 v[72:75], v[4:7], v[44:47], v[72:75]
	v_mfma_f32_16x16x32_bf16 v[76:79], v[12:15], v[44:47], v[76:79]
	v_mfma_f32_16x16x32_bf16 v[80:83], v[4:7], v[52:55], v[80:83]
	v_mfma_f32_16x16x32_bf16 v[104:107], v[12:15], v[60:63], v[84:87]
	s_setprio 0
	s_setprio 1
	v_mfma_f32_16x16x32_bf16 v[84:87], v[16:19], v[32:35], 0
	v_mfma_f32_16x16x32_bf16 v[32:35], v[24:27], v[32:35], 0
	v_mfma_f32_16x16x32_bf16 v[108:111], v[20:23], v[36:39], v[84:87]
	v_mfma_f32_16x16x32_bf16 v[32:35], v[28:31], v[36:39], v[32:35]
	v_mfma_f32_16x16x32_bf16 v[36:39], v[16:19], v[40:43], 0
	v_mfma_f32_16x16x32_bf16 v[40:43], v[24:27], v[40:43], 0
	v_mfma_f32_16x16x32_bf16 v[36:39], v[20:23], v[44:47], v[36:39]
	v_mfma_f32_16x16x32_bf16 v[40:43], v[28:31], v[44:47], v[40:43]
	v_mfma_f32_16x16x32_bf16 v[44:47], v[16:19], v[48:51], 0
	v_mfma_f32_16x16x32_bf16 v[48:51], v[24:27], v[48:51], 0
	v_mfma_f32_16x16x32_bf16 v[44:47], v[20:23], v[52:55], v[44:47]
	v_mfma_f32_16x16x32_bf16 v[48:51], v[28:31], v[52:55], v[48:51]
	v_mfma_f32_16x16x32_bf16 v[52:55], v[16:19], v[56:59], 0
	v_mfma_f32_16x16x32_bf16 v[56:59], v[24:27], v[56:59], 0
	v_mfma_f32_16x16x32_bf16 v[52:55], v[20:23], v[60:63], v[52:55]
	v_mfma_f32_16x16x32_bf16 v[56:59], v[28:31], v[60:63], v[56:59]
	s_setprio 0
	s_barrier
	s_add_i32 s55, s52, s40
	v_lshl_add_u64 v[250:251], s[30:31], 0, v[132:133]
	s_add_i32 s56, s55, 0x2000
	v_lshl_add_u64 v[158:159], v[250:251], 0, s[14:15]
	s_mov_b32 m0, s55
	v_lshl_add_u64 v[252:253], s[30:31], 0, v[128:129]
	s_add_u32 s34, s30, 0x40100
	ds_read_b128 v[60:63], v155 offset:16384
	ds_read_b128 v[84:87], v155 offset:17408
	ds_read_b128 v[96:99], v155 offset:18432
	ds_read_b128 v[100:103], v155 offset:19456
	ds_read_b128 v[112:115], v155 offset:20480
	ds_read_b128 v[116:119], v155 offset:21504
	ds_read_b128 v[120:123], v155 offset:22528
	ds_read_b128 v[124:127], v155 offset:23552
	global_load_lds_dwordx4 v[158:159], off
	v_lshl_add_u64 v[158:159], v[252:253], 0, s[14:15]
	s_mov_b32 m0, s56
	s_addc_u32 s35, s31, 0
	s_add_i32 s57, s53, s40
	global_load_lds_dwordx4 v[158:159], off
	v_lshl_add_u64 v[158:159], s[34:35], 0, v[132:133]
	s_mov_b32 m0, s57
	s_add_i32 s58, s57, 0x2000
	global_load_lds_dwordx4 v[158:159], off
	v_lshl_add_u64 v[158:159], s[34:35], 0, v[128:129]
	s_mov_b32 m0, s58
	v_lshl_add_u64 v[146:147], s[28:29], 0, v[134:135]
	global_load_lds_dwordx4 v[158:159], off
	v_lshl_add_u64 v[158:159], v[146:147], 0, s[14:15]
	s_mov_b32 m0, s43
	v_lshl_add_u64 v[148:149], s[28:29], 0, v[130:131]
	global_load_lds_dwordx4 v[158:159], off
	v_lshl_add_u64 v[158:159], v[148:149], 0, s[14:15]
	s_mov_b32 m0, s44
	s_nop 0
	global_load_lds_dwordx4 v[158:159], off
	s_waitcnt vmcnt(24)
	s_waitcnt lgkmcnt(0)
	s_barrier
	s_setprio 1
	s_waitcnt lgkmcnt(0)
	v_mfma_f32_16x16x32_bf16 v[158:161], v[0:3], v[60:63], 0
	v_mfma_f32_16x16x32_bf16 v[166:169], v[0:3], v[96:99], 0
	v_mfma_f32_16x16x32_bf16 v[174:177], v[0:3], v[112:115], 0
	v_mfma_f32_16x16x32_bf16 v[0:3], v[0:3], v[120:123], 0
	v_mfma_f32_16x16x32_bf16 v[158:161], v[4:7], v[84:87], v[158:161]
	v_mfma_f32_16x16x32_bf16 v[166:169], v[4:7], v[100:103], v[166:169]
	v_mfma_f32_16x16x32_bf16 v[174:177], v[4:7], v[116:119], v[174:177]
	v_mfma_f32_16x16x32_bf16 v[0:3], v[4:7], v[124:127], v[0:3]
	v_mfma_f32_16x16x32_bf16 v[4:7], v[8:11], v[120:123], 0
	v_mfma_f32_16x16x32_bf16 v[162:165], v[8:11], v[60:63], 0
	v_mfma_f32_16x16x32_bf16 v[170:173], v[8:11], v[96:99], 0
	v_mfma_f32_16x16x32_bf16 v[178:181], v[8:11], v[112:115], 0
	v_mfma_f32_16x16x32_bf16 v[8:11], v[12:15], v[124:127], v[4:7]
	v_mfma_f32_16x16x32_bf16 v[162:165], v[12:15], v[84:87], v[162:165]
	v_mfma_f32_16x16x32_bf16 v[170:173], v[12:15], v[100:103], v[170:173]
	v_mfma_f32_16x16x32_bf16 v[178:181], v[12:15], v[116:119], v[178:181]
	s_setprio 0
	s_setprio 1
	v_mfma_f32_16x16x32_bf16 v[4:7], v[16:19], v[60:63], 0
	v_mfma_f32_16x16x32_bf16 v[12:15], v[20:23], v[84:87], v[4:7]
	v_mfma_f32_16x16x32_bf16 v[4:7], v[24:27], v[60:63], 0
	v_mfma_f32_16x16x32_bf16 v[182:185], v[28:31], v[84:87], v[4:7]
	v_mfma_f32_16x16x32_bf16 v[4:7], v[16:19], v[96:99], 0
	v_mfma_f32_16x16x32_bf16 v[186:189], v[20:23], v[100:103], v[4:7]
	v_mfma_f32_16x16x32_bf16 v[4:7], v[24:27], v[96:99], 0
	v_mfma_f32_16x16x32_bf16 v[190:193], v[28:31], v[100:103], v[4:7]
	v_mfma_f32_16x16x32_bf16 v[4:7], v[16:19], v[112:115], 0
	v_mfma_f32_16x16x32_bf16 v[194:197], v[20:23], v[116:119], v[4:7]
	v_mfma_f32_16x16x32_bf16 v[4:7], v[24:27], v[112:115], 0
	v_mfma_f32_16x16x32_bf16 v[198:201], v[28:31], v[116:119], v[4:7]
	v_mfma_f32_16x16x32_bf16 v[4:7], v[16:19], v[120:123], 0
	v_mfma_f32_16x16x32_bf16 v[202:205], v[20:23], v[124:127], v[4:7]
	v_mfma_f32_16x16x32_bf16 v[4:7], v[24:27], v[120:123], 0
	v_mfma_f32_16x16x32_bf16 v[206:209], v[28:31], v[124:127], v[4:7]
	s_setprio 0
	s_barrier
	s_add_i32 s59, 0, 0x18000
	s_add_i32 s61, 0, 0x1c000
	v_add_u32_e32 v136, s59, v150
	v_add_u32_e32 v157, s61, v150
	s_nop 0
	ds_read_b128 v[4:7], v136
	ds_read_b128 v[24:27], v136 offset:1024
	ds_read_b128 v[28:31], v136 offset:2048
	ds_read_b128 v[60:63], v136 offset:3072
	ds_read_b128 v[210:213], v157
	ds_read_b128 v[214:217], v157 offset:1024
	ds_read_b128 v[218:221], v157 offset:2048
	ds_read_b128 v[222:225], v157 offset:3072
	s_add_u32 s34, s28, 0x40100
	s_addc_u32 s35, s29, 0
	s_mov_b32 m0, s45
	v_lshl_add_u64 v[84:85], s[34:35], 0, v[134:135]
	ds_read_b128 v[16:19], v155 offset:32768
	ds_read_b128 v[20:23], v155 offset:33792
	ds_read_b128 v[226:229], v155 offset:34816
	ds_read_b128 v[230:233], v155 offset:35840
	ds_read_b128 v[234:237], v155 offset:36864
	ds_read_b128 v[238:241], v155 offset:37888
	ds_read_b128 v[242:245], v155 offset:38912
	ds_read_b128 v[246:249], v155 offset:39936
	global_load_lds_dwordx4 v[84:85], off
	v_lshl_add_u64 v[84:85], s[34:35], 0, v[130:131]
	s_mov_b32 m0, s46
	s_nop 0
	global_load_lds_dwordx4 v[84:85], off
	s_waitcnt vmcnt(8)
	s_waitcnt lgkmcnt(0)
	s_barrier
	s_setprio 1
	s_waitcnt lgkmcnt(0)
	v_mfma_f32_16x16x32_bf16 v[64:67], v[4:7], v[16:19], v[64:67]
	v_mfma_f32_16x16x32_bf16 v[116:119], v[24:27], v[20:23], v[64:67]
	v_mfma_f32_16x16x32_bf16 v[64:67], v[28:31], v[16:19], v[68:71]
	v_mfma_f32_16x16x32_bf16 v[112:115], v[60:63], v[20:23], v[64:67]
	v_mfma_f32_16x16x32_bf16 v[64:67], v[4:7], v[226:229], v[72:75]
	v_mfma_f32_16x16x32_bf16 v[100:103], v[24:27], v[230:233], v[64:67]
	v_mfma_f32_16x16x32_bf16 v[64:67], v[28:31], v[226:229], v[76:79]
	v_mfma_f32_16x16x32_bf16 v[96:99], v[60:63], v[230:233], v[64:67]
	v_mfma_f32_16x16x32_bf16 v[64:67], v[4:7], v[234:237], v[80:83]
	v_mfma_f32_16x16x32_bf16 v[84:87], v[24:27], v[238:241], v[64:67]
	v_mfma_f32_16x16x32_bf16 v[64:67], v[28:31], v[234:237], v[88:91]
	v_mfma_f32_16x16x32_bf16 v[80:83], v[60:63], v[238:241], v[64:67]
	v_mfma_f32_16x16x32_bf16 v[64:67], v[4:7], v[242:245], v[92:95]
	v_mfma_f32_16x16x32_bf16 v[68:71], v[24:27], v[246:249], v[64:67]
	v_mfma_f32_16x16x32_bf16 v[64:67], v[28:31], v[242:245], v[104:107]
	v_mfma_f32_16x16x32_bf16 v[64:67], v[60:63], v[246:249], v[64:67]
	s_setprio 0
	s_setprio 1
	v_mfma_f32_16x16x32_bf16 v[72:75], v[210:213], v[16:19], v[108:111]
	v_mfma_f32_16x16x32_bf16 v[16:19], v[218:221], v[16:19], v[32:35]
	v_mfma_f32_16x16x32_bf16 v[120:123], v[222:225], v[20:23], v[16:19]
	v_mfma_f32_16x16x32_bf16 v[16:19], v[210:213], v[226:229], v[36:39]
	v_mfma_f32_16x16x32_bf16 v[108:111], v[214:217], v[230:233], v[16:19]
	v_mfma_f32_16x16x32_bf16 v[16:19], v[218:221], v[226:229], v[40:43]
	v_mfma_f32_16x16x32_bf16 v[104:107], v[222:225], v[230:233], v[16:19]
	v_mfma_f32_16x16x32_bf16 v[16:19], v[210:213], v[234:237], v[44:47]
	v_mfma_f32_16x16x32_bf16 v[92:95], v[214:217], v[238:241], v[16:19]
	v_mfma_f32_16x16x32_bf16 v[16:19], v[218:221], v[234:237], v[48:51]
	v_mfma_f32_16x16x32_bf16 v[88:91], v[222:225], v[238:241], v[16:19]
	v_mfma_f32_16x16x32_bf16 v[16:19], v[210:213], v[242:245], v[52:55]
	v_mfma_f32_16x16x32_bf16 v[76:79], v[214:217], v[246:249], v[16:19]
	v_mfma_f32_16x16x32_bf16 v[16:19], v[218:221], v[242:245], v[56:59]
	v_mfma_f32_16x16x32_bf16 v[124:127], v[214:217], v[20:23], v[72:75]
	v_mfma_f32_16x16x32_bf16 v[72:75], v[222:225], v[246:249], v[16:19]
	s_setprio 0
	s_barrier
	s_add_i32 s59, s59, s40
	s_add_i32 s60, s59, 0x2000
	s_nop 1
	v_lshl_add_u64 v[16:17], v[250:251], 0, s[16:17]
	s_mov_b32 m0, s59
	s_add_u32 s34, s30, 0x40180
	ds_read_b128 v[40:43], v155 offset:49152
	ds_read_b128 v[44:47], v155 offset:50176
	ds_read_b128 v[226:229], v155 offset:51200
	ds_read_b128 v[230:233], v155 offset:52224
	ds_read_b128 v[234:237], v155 offset:53248
	ds_read_b128 v[238:241], v155 offset:54272
	ds_read_b128 v[242:245], v155 offset:55296
	ds_read_b128 v[246:249], v155 offset:56320
	global_load_lds_dwordx4 v[16:17], off
	v_lshl_add_u64 v[16:17], v[252:253], 0, s[16:17]
	s_mov_b32 m0, s60
	s_addc_u32 s35, s31, 0
	s_add_i32 s61, s61, s40
	global_load_lds_dwordx4 v[16:17], off
	v_lshl_add_u64 v[16:17], s[34:35], 0, v[132:133]
	s_mov_b32 m0, s61
	s_add_i32 s62, s61, 0x2000
	global_load_lds_dwordx4 v[16:17], off
	v_lshl_add_u64 v[16:17], s[34:35], 0, v[128:129]
	s_mov_b32 m0, s62
	s_nop 0
	global_load_lds_dwordx4 v[16:17], off
	v_lshl_add_u64 v[16:17], v[146:147], 0, s[16:17]
	s_mov_b32 m0, s48
	s_nop 0
	global_load_lds_dwordx4 v[16:17], off
	v_lshl_add_u64 v[16:17], v[148:149], 0, s[16:17]
	s_mov_b32 m0, s49
	s_nop 0
	global_load_lds_dwordx4 v[16:17], off
	s_waitcnt vmcnt(8)
	s_waitcnt lgkmcnt(0)
	s_barrier
	s_setprio 1
	s_waitcnt lgkmcnt(0)
	v_mfma_f32_16x16x32_bf16 v[16:19], v[4:7], v[40:43], v[158:161]
	v_mfma_f32_16x16x32_bf16 v[52:55], v[24:27], v[44:47], v[16:19]
	v_mfma_f32_16x16x32_bf16 v[16:19], v[28:31], v[40:43], v[162:165]
	v_mfma_f32_16x16x32_bf16 v[48:51], v[60:63], v[44:47], v[16:19]
	v_mfma_f32_16x16x32_bf16 v[16:19], v[4:7], v[226:229], v[166:169]
	v_mfma_f32_16x16x32_bf16 v[36:39], v[24:27], v[230:233], v[16:19]
	v_mfma_f32_16x16x32_bf16 v[16:19], v[28:31], v[226:229], v[170:173]
	v_mfma_f32_16x16x32_bf16 v[32:35], v[60:63], v[230:233], v[16:19]
	v_mfma_f32_16x16x32_bf16 v[16:19], v[4:7], v[234:237], v[174:177]
	v_mfma_f32_16x16x32_bf16 v[0:3], v[4:7], v[242:245], v[0:3]
	v_mfma_f32_16x16x32_bf16 v[20:23], v[24:27], v[238:241], v[16:19]
	v_mfma_f32_16x16x32_bf16 v[16:19], v[28:31], v[234:237], v[178:181]
	v_mfma_f32_16x16x32_bf16 v[4:7], v[24:27], v[246:249], v[0:3]
	v_mfma_f32_16x16x32_bf16 v[0:3], v[28:31], v[242:245], v[8:11]
	v_mfma_f32_16x16x32_bf16 v[16:19], v[60:63], v[238:241], v[16:19]
	v_mfma_f32_16x16x32_bf16 v[0:3], v[60:63], v[246:249], v[0:3]
	s_setprio 0
	s_setprio 1
	v_mfma_f32_16x16x32_bf16 v[8:11], v[210:213], v[40:43], v[12:15]
	v_mfma_f32_16x16x32_bf16 v[60:63], v[214:217], v[44:47], v[8:11]
	v_mfma_f32_16x16x32_bf16 v[8:11], v[218:221], v[40:43], v[182:185]
	v_mfma_f32_16x16x32_bf16 v[56:59], v[222:225], v[44:47], v[8:11]
	v_mfma_f32_16x16x32_bf16 v[8:11], v[210:213], v[226:229], v[186:189]
	v_mfma_f32_16x16x32_bf16 v[44:47], v[214:217], v[230:233], v[8:11]
	v_mfma_f32_16x16x32_bf16 v[8:11], v[218:221], v[226:229], v[190:193]
	v_mfma_f32_16x16x32_bf16 v[40:43], v[222:225], v[230:233], v[8:11]
	v_mfma_f32_16x16x32_bf16 v[8:11], v[210:213], v[234:237], v[194:197]
	v_mfma_f32_16x16x32_bf16 v[28:31], v[214:217], v[238:241], v[8:11]
	v_mfma_f32_16x16x32_bf16 v[8:11], v[218:221], v[234:237], v[198:201]
	v_mfma_f32_16x16x32_bf16 v[24:27], v[222:225], v[238:241], v[8:11]
	v_mfma_f32_16x16x32_bf16 v[8:11], v[210:213], v[242:245], v[202:205]
	v_mfma_f32_16x16x32_bf16 v[12:15], v[214:217], v[246:249], v[8:11]
	v_mfma_f32_16x16x32_bf16 v[8:11], v[218:221], v[242:245], v[206:209]
	v_mfma_f32_16x16x32_bf16 v[8:11], v[222:225], v[246:249], v[8:11]
	s_setprio 0
	s_barrier
	s_add_u32 s63, s30, 0x200
	s_addc_u32 s64, s31, 0
	s_add_u32 s28, s28, 0x40180
	s_addc_u32 s29, s29, 0
	s_mov_b32 s65, 0
	s_cmp_lt_u32 s96, 4
	s_cbranch_scc1 .Lprio_skip_271
	s_setprio 1
.Lprio_skip_271:
.LBB0_271:
	ds_read_b128 v[158:161], v153
	ds_read_b128 v[162:165], v153 offset:1024
	ds_read_b128 v[166:169], v153 offset:2048
	ds_read_b128 v[170:173], v153 offset:3072
	ds_read_b128 v[174:177], v154
	ds_read_b128 v[178:181], v154 offset:1024
	ds_read_b128 v[182:185], v154 offset:2048
	ds_read_b128 v[186:189], v154 offset:3072
	s_add_u32 s30, s28, 0xfffc0080
	s_addc_u32 s31, s29, -1
	s_cmp_eq_u32 s65, 12
	s_cselect_b32 s35, s23, s31
	s_cselect_b32 s34, s22, s30
	s_cselect_b32 s31, s25, s64
	s_cselect_b32 s30, s24, s63
	s_mov_b32 m0, s19
	ds_read_b128 v[190:193], v155
	ds_read_b128 v[194:197], v155 offset:1024
	ds_read_b128 v[198:201], v155 offset:2048
	ds_read_b128 v[202:205], v155 offset:3072
	ds_read_b128 v[206:209], v155 offset:4096
	ds_read_b128 v[210:213], v155 offset:5120
	ds_read_b128 v[214:217], v155 offset:6144
	ds_read_b128 v[218:221], v155 offset:7168
	global_load_lds_dwordx4 v144, s[28:29]
	s_mov_b32 m0, s21
	s_nop 0
	global_load_lds_dwordx4 v142, s[28:29]
	s_waitcnt vmcnt(8)
	s_waitcnt lgkmcnt(0)
	s_barrier
	s_waitcnt lgkmcnt(0)
	v_mfma_f32_16x16x32_bf16 v[116:119], v[158:161], v[190:193], v[116:119]
	v_mfma_f32_16x16x32_bf16 v[112:115], v[166:169], v[190:193], v[112:115]
	v_mfma_f32_16x16x32_bf16 v[100:103], v[158:161], v[198:201], v[100:103]
	v_mfma_f32_16x16x32_bf16 v[96:99], v[166:169], v[198:201], v[96:99]
	v_mfma_f32_16x16x32_bf16 v[84:87], v[158:161], v[206:209], v[84:87]
	v_mfma_f32_16x16x32_bf16 v[80:83], v[166:169], v[206:209], v[80:83]
	v_mfma_f32_16x16x32_bf16 v[68:71], v[158:161], v[214:217], v[68:71]
	v_mfma_f32_16x16x32_bf16 v[64:67], v[166:169], v[214:217], v[64:67]
	v_mfma_f32_16x16x32_bf16 v[116:119], v[162:165], v[194:197], v[116:119]
	v_mfma_f32_16x16x32_bf16 v[112:115], v[170:173], v[194:197], v[112:115]
	v_mfma_f32_16x16x32_bf16 v[100:103], v[162:165], v[202:205], v[100:103]
	v_mfma_f32_16x16x32_bf16 v[96:99], v[170:173], v[202:205], v[96:99]
	v_mfma_f32_16x16x32_bf16 v[84:87], v[162:165], v[210:213], v[84:87]
	v_mfma_f32_16x16x32_bf16 v[80:83], v[170:173], v[210:213], v[80:83]
	v_mfma_f32_16x16x32_bf16 v[68:71], v[162:165], v[218:221], v[68:71]
	v_mfma_f32_16x16x32_bf16 v[64:67], v[170:173], v[218:221], v[64:67]
	v_mfma_f32_16x16x32_bf16 v[124:127], v[174:177], v[190:193], v[124:127]
	v_mfma_f32_16x16x32_bf16 v[120:123], v[182:185], v[190:193], v[120:123]
	v_mfma_f32_16x16x32_bf16 v[108:111], v[174:177], v[198:201], v[108:111]
	v_mfma_f32_16x16x32_bf16 v[104:107], v[182:185], v[198:201], v[104:107]
	v_mfma_f32_16x16x32_bf16 v[92:95], v[174:177], v[206:209], v[92:95]
	v_mfma_f32_16x16x32_bf16 v[88:91], v[182:185], v[206:209], v[88:91]
	v_mfma_f32_16x16x32_bf16 v[76:79], v[174:177], v[214:217], v[76:79]
	v_mfma_f32_16x16x32_bf16 v[72:75], v[182:185], v[214:217], v[72:75]
	v_mfma_f32_16x16x32_bf16 v[124:127], v[178:181], v[194:197], v[124:127]
	v_mfma_f32_16x16x32_bf16 v[120:123], v[186:189], v[194:197], v[120:123]
	v_mfma_f32_16x16x32_bf16 v[108:111], v[178:181], v[202:205], v[108:111]
	v_mfma_f32_16x16x32_bf16 v[104:107], v[186:189], v[202:205], v[104:107]
	v_mfma_f32_16x16x32_bf16 v[92:95], v[178:181], v[210:213], v[92:95]
	v_mfma_f32_16x16x32_bf16 v[88:91], v[186:189], v[210:213], v[88:91]
	v_mfma_f32_16x16x32_bf16 v[76:79], v[178:181], v[218:221], v[76:79]
	v_mfma_f32_16x16x32_bf16 v[72:75], v[186:189], v[218:221], v[72:75]
	s_barrier
	s_mov_b32 m0, s55
	s_add_u32 s66, s30, 0x40000
	ds_read_b128 v[190:193], v155 offset:16384
	ds_read_b128 v[194:197], v155 offset:17408
	ds_read_b128 v[198:201], v155 offset:18432
	ds_read_b128 v[202:205], v155 offset:19456
	ds_read_b128 v[206:209], v155 offset:20480
	ds_read_b128 v[210:213], v155 offset:21504
	ds_read_b128 v[214:217], v155 offset:22528
	ds_read_b128 v[218:221], v155 offset:23552
	global_load_lds_dwordx4 v132, s[30:31]
	s_mov_b32 m0, s56
	s_addc_u32 s67, s31, 0
	global_load_lds_dwordx4 v128, s[30:31]
	s_mov_b32 m0, s57
	s_nop 0
	global_load_lds_dwordx4 v132, s[66:67]
	s_mov_b32 m0, s58
	s_nop 0
	global_load_lds_dwordx4 v128, s[66:67]
	s_mov_b32 m0, s43
	s_nop 0
	global_load_lds_dwordx4 v134, s[34:35]
	s_mov_b32 m0, s44
	s_nop 0
	global_load_lds_dwordx4 v130, s[34:35]
	s_waitcnt vmcnt(8)
	s_waitcnt lgkmcnt(0)
	s_barrier
	s_waitcnt lgkmcnt(0)
	v_mfma_f32_16x16x32_bf16 v[52:55], v[158:161], v[190:193], v[52:55]
	v_mfma_f32_16x16x32_bf16 v[48:51], v[166:169], v[190:193], v[48:51]
	v_mfma_f32_16x16x32_bf16 v[36:39], v[158:161], v[198:201], v[36:39]
	v_mfma_f32_16x16x32_bf16 v[32:35], v[166:169], v[198:201], v[32:35]
	v_mfma_f32_16x16x32_bf16 v[20:23], v[158:161], v[206:209], v[20:23]
	v_mfma_f32_16x16x32_bf16 v[16:19], v[166:169], v[206:209], v[16:19]
	v_mfma_f32_16x16x32_bf16 v[4:7], v[158:161], v[214:217], v[4:7]
	v_mfma_f32_16x16x32_bf16 v[0:3], v[166:169], v[214:217], v[0:3]
	v_mfma_f32_16x16x32_bf16 v[52:55], v[162:165], v[194:197], v[52:55]
	v_mfma_f32_16x16x32_bf16 v[48:51], v[170:173], v[194:197], v[48:51]
	v_mfma_f32_16x16x32_bf16 v[36:39], v[162:165], v[202:205], v[36:39]
	v_mfma_f32_16x16x32_bf16 v[32:35], v[170:173], v[202:205], v[32:35]
	v_mfma_f32_16x16x32_bf16 v[20:23], v[162:165], v[210:213], v[20:23]
	v_mfma_f32_16x16x32_bf16 v[16:19], v[170:173], v[210:213], v[16:19]
	v_mfma_f32_16x16x32_bf16 v[4:7], v[162:165], v[218:221], v[4:7]
	v_mfma_f32_16x16x32_bf16 v[0:3], v[170:173], v[218:221], v[0:3]
	v_mfma_f32_16x16x32_bf16 v[60:63], v[174:177], v[190:193], v[60:63]
	v_mfma_f32_16x16x32_bf16 v[56:59], v[182:185], v[190:193], v[56:59]
	v_mfma_f32_16x16x32_bf16 v[44:47], v[174:177], v[198:201], v[44:47]
	v_mfma_f32_16x16x32_bf16 v[40:43], v[182:185], v[198:201], v[40:43]
	v_mfma_f32_16x16x32_bf16 v[28:31], v[174:177], v[206:209], v[28:31]
	v_mfma_f32_16x16x32_bf16 v[24:27], v[182:185], v[206:209], v[24:27]
	v_mfma_f32_16x16x32_bf16 v[12:15], v[174:177], v[214:217], v[12:15]
	v_mfma_f32_16x16x32_bf16 v[8:11], v[182:185], v[214:217], v[8:11]
	v_mfma_f32_16x16x32_bf16 v[60:63], v[178:181], v[194:197], v[60:63]
	v_mfma_f32_16x16x32_bf16 v[56:59], v[186:189], v[194:197], v[56:59]
	v_mfma_f32_16x16x32_bf16 v[44:47], v[178:181], v[202:205], v[44:47]
	v_mfma_f32_16x16x32_bf16 v[40:43], v[186:189], v[202:205], v[40:43]
	v_mfma_f32_16x16x32_bf16 v[28:31], v[178:181], v[210:213], v[28:31]
	v_mfma_f32_16x16x32_bf16 v[24:27], v[186:189], v[210:213], v[24:27]
	v_mfma_f32_16x16x32_bf16 v[12:15], v[178:181], v[218:221], v[12:15]
	v_mfma_f32_16x16x32_bf16 v[8:11], v[186:189], v[218:221], v[8:11]
	s_barrier
	ds_read_b128 v[158:161], v136
	ds_read_b128 v[162:165], v136 offset:1024
	ds_read_b128 v[166:169], v136 offset:2048
	ds_read_b128 v[170:173], v136 offset:3072
	ds_read_b128 v[174:177], v157
	ds_read_b128 v[178:181], v157 offset:1024
	ds_read_b128 v[182:185], v157 offset:2048
	ds_read_b128 v[186:189], v157 offset:3072
	s_add_u32 s98, s34, 0x80
	s_addc_u32 s99, s35, 0
	s_add_u32 s34, s34, 0x40000
	s_addc_u32 s35, s35, 0
	s_mov_b32 m0, s45
	ds_read_b128 v[190:193], v155 offset:32768
	ds_read_b128 v[194:197], v155 offset:33792
	ds_read_b128 v[198:201], v155 offset:34816
	ds_read_b128 v[202:205], v155 offset:35840
	ds_read_b128 v[206:209], v155 offset:36864
	ds_read_b128 v[210:213], v155 offset:37888
	ds_read_b128 v[214:217], v155 offset:38912
	ds_read_b128 v[218:221], v155 offset:39936
	global_load_lds_dwordx4 v134, s[34:35]
	s_mov_b32 m0, s46
	s_nop 0
	global_load_lds_dwordx4 v130, s[34:35]
	s_waitcnt vmcnt(8)
	s_waitcnt lgkmcnt(0)
	s_barrier
	s_waitcnt lgkmcnt(0)
	v_mfma_f32_16x16x32_bf16 v[116:119], v[158:161], v[190:193], v[116:119]
	v_mfma_f32_16x16x32_bf16 v[112:115], v[166:169], v[190:193], v[112:115]
	v_mfma_f32_16x16x32_bf16 v[100:103], v[158:161], v[198:201], v[100:103]
	v_mfma_f32_16x16x32_bf16 v[96:99], v[166:169], v[198:201], v[96:99]
	v_mfma_f32_16x16x32_bf16 v[84:87], v[158:161], v[206:209], v[84:87]
	v_mfma_f32_16x16x32_bf16 v[80:83], v[166:169], v[206:209], v[80:83]
	v_mfma_f32_16x16x32_bf16 v[68:71], v[158:161], v[214:217], v[68:71]
	v_mfma_f32_16x16x32_bf16 v[64:67], v[166:169], v[214:217], v[64:67]
	v_mfma_f32_16x16x32_bf16 v[116:119], v[162:165], v[194:197], v[116:119]
	v_mfma_f32_16x16x32_bf16 v[112:115], v[170:173], v[194:197], v[112:115]
	v_mfma_f32_16x16x32_bf16 v[100:103], v[162:165], v[202:205], v[100:103]
	v_mfma_f32_16x16x32_bf16 v[96:99], v[170:173], v[202:205], v[96:99]
	v_mfma_f32_16x16x32_bf16 v[84:87], v[162:165], v[210:213], v[84:87]
	v_mfma_f32_16x16x32_bf16 v[80:83], v[170:173], v[210:213], v[80:83]
	v_mfma_f32_16x16x32_bf16 v[68:71], v[162:165], v[218:221], v[68:71]
	v_mfma_f32_16x16x32_bf16 v[64:67], v[170:173], v[218:221], v[64:67]
	v_mfma_f32_16x16x32_bf16 v[124:127], v[174:177], v[190:193], v[124:127]
	v_mfma_f32_16x16x32_bf16 v[120:123], v[182:185], v[190:193], v[120:123]
	v_mfma_f32_16x16x32_bf16 v[108:111], v[174:177], v[198:201], v[108:111]
	v_mfma_f32_16x16x32_bf16 v[104:107], v[182:185], v[198:201], v[104:107]
	v_mfma_f32_16x16x32_bf16 v[92:95], v[174:177], v[206:209], v[92:95]
	v_mfma_f32_16x16x32_bf16 v[88:91], v[182:185], v[206:209], v[88:91]
	v_mfma_f32_16x16x32_bf16 v[76:79], v[174:177], v[214:217], v[76:79]
	v_mfma_f32_16x16x32_bf16 v[72:75], v[182:185], v[214:217], v[72:75]
	v_mfma_f32_16x16x32_bf16 v[124:127], v[178:181], v[194:197], v[124:127]
	v_mfma_f32_16x16x32_bf16 v[120:123], v[186:189], v[194:197], v[120:123]
	v_mfma_f32_16x16x32_bf16 v[108:111], v[178:181], v[202:205], v[108:111]
	v_mfma_f32_16x16x32_bf16 v[104:107], v[186:189], v[202:205], v[104:107]
	v_mfma_f32_16x16x32_bf16 v[92:95], v[178:181], v[210:213], v[92:95]
	v_mfma_f32_16x16x32_bf16 v[88:91], v[186:189], v[210:213], v[88:91]
	v_mfma_f32_16x16x32_bf16 v[76:79], v[178:181], v[218:221], v[76:79]
	v_mfma_f32_16x16x32_bf16 v[72:75], v[186:189], v[218:221], v[72:75]
	s_barrier
	s_mov_b32 m0, s59
	s_add_u32 s100, s30, 0x80
	s_addc_u32 s101, s31, 0
	ds_read_b128 v[190:193], v155 offset:49152
	ds_read_b128 v[194:197], v155 offset:50176
	ds_read_b128 v[198:201], v155 offset:51200
	ds_read_b128 v[202:205], v155 offset:52224
	ds_read_b128 v[206:209], v155 offset:53248
	ds_read_b128 v[210:213], v155 offset:54272
	ds_read_b128 v[214:217], v155 offset:55296
	ds_read_b128 v[218:221], v155 offset:56320
	global_load_lds_dwordx4 v132, s[100:101]
	s_mov_b32 m0, s60
	s_nop 0
	global_load_lds_dwordx4 v128, s[100:101]
	s_add_u32 s30, s30, 0x40080
	s_addc_u32 s31, s31, 0
	s_mov_b32 m0, s61
	s_nop 0
	global_load_lds_dwordx4 v132, s[30:31]
	s_mov_b32 m0, s62
	s_nop 0
	global_load_lds_dwordx4 v128, s[30:31]
	s_mov_b32 m0, s48
	s_nop 0
	global_load_lds_dwordx4 v134, s[98:99]
	s_mov_b32 m0, s49
	s_nop 0
	global_load_lds_dwordx4 v130, s[98:99]
	s_waitcnt vmcnt(8)
	s_waitcnt lgkmcnt(0)
	s_barrier
	s_waitcnt lgkmcnt(0)
	v_mfma_f32_16x16x32_bf16 v[52:55], v[158:161], v[190:193], v[52:55]
	v_mfma_f32_16x16x32_bf16 v[48:51], v[166:169], v[190:193], v[48:51]
	v_mfma_f32_16x16x32_bf16 v[36:39], v[158:161], v[198:201], v[36:39]
	v_mfma_f32_16x16x32_bf16 v[32:35], v[166:169], v[198:201], v[32:35]
	v_mfma_f32_16x16x32_bf16 v[20:23], v[158:161], v[206:209], v[20:23]
	v_mfma_f32_16x16x32_bf16 v[16:19], v[166:169], v[206:209], v[16:19]
	v_mfma_f32_16x16x32_bf16 v[4:7], v[158:161], v[214:217], v[4:7]
	v_mfma_f32_16x16x32_bf16 v[0:3], v[166:169], v[214:217], v[0:3]
	v_mfma_f32_16x16x32_bf16 v[52:55], v[162:165], v[194:197], v[52:55]
	v_mfma_f32_16x16x32_bf16 v[48:51], v[170:173], v[194:197], v[48:51]
	v_mfma_f32_16x16x32_bf16 v[36:39], v[162:165], v[202:205], v[36:39]
	v_mfma_f32_16x16x32_bf16 v[32:35], v[170:173], v[202:205], v[32:35]
	v_mfma_f32_16x16x32_bf16 v[20:23], v[162:165], v[210:213], v[20:23]
	v_mfma_f32_16x16x32_bf16 v[16:19], v[170:173], v[210:213], v[16:19]
	v_mfma_f32_16x16x32_bf16 v[4:7], v[162:165], v[218:221], v[4:7]
	v_mfma_f32_16x16x32_bf16 v[0:3], v[170:173], v[218:221], v[0:3]
	v_mfma_f32_16x16x32_bf16 v[60:63], v[174:177], v[190:193], v[60:63]
	v_mfma_f32_16x16x32_bf16 v[56:59], v[182:185], v[190:193], v[56:59]
	v_mfma_f32_16x16x32_bf16 v[44:47], v[174:177], v[198:201], v[44:47]
	v_mfma_f32_16x16x32_bf16 v[40:43], v[182:185], v[198:201], v[40:43]
	v_mfma_f32_16x16x32_bf16 v[28:31], v[174:177], v[206:209], v[28:31]
	v_mfma_f32_16x16x32_bf16 v[24:27], v[182:185], v[206:209], v[24:27]
	v_mfma_f32_16x16x32_bf16 v[12:15], v[174:177], v[214:217], v[12:15]
	v_mfma_f32_16x16x32_bf16 v[8:11], v[182:185], v[214:217], v[8:11]
	v_mfma_f32_16x16x32_bf16 v[60:63], v[178:181], v[194:197], v[60:63]
	v_mfma_f32_16x16x32_bf16 v[56:59], v[186:189], v[194:197], v[56:59]
	v_mfma_f32_16x16x32_bf16 v[44:47], v[178:181], v[202:205], v[44:47]
	v_mfma_f32_16x16x32_bf16 v[40:43], v[186:189], v[202:205], v[40:43]
	v_mfma_f32_16x16x32_bf16 v[28:31], v[178:181], v[210:213], v[28:31]
	v_mfma_f32_16x16x32_bf16 v[24:27], v[186:189], v[210:213], v[24:27]
	v_mfma_f32_16x16x32_bf16 v[12:15], v[178:181], v[218:221], v[12:15]
	v_mfma_f32_16x16x32_bf16 v[8:11], v[186:189], v[218:221], v[8:11]
	s_barrier
	s_add_i32 s65, s65, 2
	s_add_u32 s63, s63, 0x100
	s_addc_u32 s64, s64, 0
	s_add_u32 s28, s28, 0x100
	s_addc_u32 s29, s29, 0
	s_cmp_gt_u32 s65, 13
	s_cbranch_scc0 .LBB0_271
	s_setprio 0
	s_and_b64 vcc, exec, s[12:13]
	s_cbranch_vccz .LBB0_274
	s_barrier
